# v44 + prologue b1f loop in 4 round trips (no row prefetch), later code kept at v44's byte phase
# speedup vs baseline: 1.0134x; 1.0101x over previous
; __device__ __forceinline__ void prologue(const Ctx& C, const In& I, unsigned char* ws, bf16* hs0) {
;     ...
;     for (int w = C.ngw - 1 - C.gw; w < 256; w += C.ngw) {
;         const int e0 = 4 * w, jk = e0 >> 8, col = (e0 & 255) + (C.lane & 3), ks = C.lane >> 2;
;         const float* pe = I.nsa_pe + (size_t)jk * 2048 + 128 * ks; const float* w1 = I.nsa_w1 + (size_t)jk * 2048 * 256 + (size_t)(128 * ks) * 256 + col; float sacc = 0.f;
; #pragma unroll 8
;         for (int i = 0; i < 128; ++i) sacc += pe[i] * w1[(size_t)i * 256];
;         sacc += __shfl_xor(sacc, 4); sacc += __shfl_xor(sacc, 8); sacc += __shfl_xor(sacc, 16); sacc += __shfl_xor(sacc, 32);
;         if (C.lane < 4) b1f[e0 + C.lane] = sacc + I.nsa_b1[e0 + C.lane];
.LBB0_81:
	v_lshl_add_u64 v[20:21], v[6:7], 0, s[12:13]
	s_add_u32 s12, s12, 0x80
	s_addc_u32 s13, s13, 0
	global_load_dwordx4 v[64:67], v[20:21], off offset:0
	global_load_dwordx4 v[68:71], v[20:21], off offset:16
	v_add_co_u32_e32 v24, vcc, 0xfffff000, v8
	s_nop 1
	v_addc_co_u32_e32 v25, vcc, -1, v9, vcc
	global_load_dword v72, v[24:25], off offset:-3072
	global_load_dword v73, v[24:25], off offset:-2048
	global_load_dword v74, v[24:25], off offset:-1024
	global_load_dword v75, v[8:9], off offset:-4096
	global_load_dword v76, v[8:9], off offset:-3072
	global_load_dword v77, v[8:9], off offset:-2048
	global_load_dword v78, v[8:9], off offset:-1024
	global_load_dword v79, v[8:9], off
	v_lshl_add_u64 v[128:129], v[8:9], 0, s[10:11]
	global_load_dwordx4 v[80:83], v[20:21], off offset:32
	global_load_dwordx4 v[84:87], v[20:21], off offset:48
	v_add_co_u32_e32 v134, vcc, 0xfffff000, v128
	s_nop 1
	v_addc_co_u32_e32 v135, vcc, -1, v129, vcc
	global_load_dword v88, v[134:135], off offset:-3072
	global_load_dword v89, v[134:135], off offset:-2048
	global_load_dword v90, v[134:135], off offset:-1024
	global_load_dword v91, v[128:129], off offset:-4096
	global_load_dword v92, v[128:129], off offset:-3072
	global_load_dword v93, v[128:129], off offset:-2048
	global_load_dword v94, v[128:129], off offset:-1024
	global_load_dword v95, v[128:129], off
	v_lshl_add_u64 v[130:131], v[128:129], 0, s[10:11]
	global_load_dwordx4 v[96:99], v[20:21], off offset:64
	global_load_dwordx4 v[100:103], v[20:21], off offset:80
	v_add_co_u32_e32 v136, vcc, 0xfffff000, v130
	s_nop 1
	v_addc_co_u32_e32 v137, vcc, -1, v131, vcc
	global_load_dword v104, v[136:137], off offset:-3072
	global_load_dword v105, v[136:137], off offset:-2048
	global_load_dword v106, v[136:137], off offset:-1024
	global_load_dword v107, v[130:131], off offset:-4096
	global_load_dword v108, v[130:131], off offset:-3072
	global_load_dword v109, v[130:131], off offset:-2048
	global_load_dword v110, v[130:131], off offset:-1024
	global_load_dword v111, v[130:131], off
	v_lshl_add_u64 v[132:133], v[130:131], 0, s[10:11]
	global_load_dwordx4 v[112:115], v[20:21], off offset:96
	global_load_dwordx4 v[116:119], v[20:21], off offset:112
	v_add_co_u32_e32 v138, vcc, 0xfffff000, v132
	s_nop 1
	v_addc_co_u32_e32 v139, vcc, -1, v133, vcc
	global_load_dword v120, v[138:139], off offset:-3072
	global_load_dword v121, v[138:139], off offset:-2048
	global_load_dword v122, v[138:139], off offset:-1024
	global_load_dword v123, v[132:133], off offset:-4096
	global_load_dword v124, v[132:133], off offset:-3072
	global_load_dword v125, v[132:133], off offset:-2048
	global_load_dword v126, v[132:133], off offset:-1024
	global_load_dword v127, v[132:133], off
	v_lshl_add_u64 v[8:9], v[132:133], 0, s[10:11]
	s_waitcnt vmcnt(0)
	v_fmac_f32_e32 v15, v64, v72
	v_fmac_f32_e32 v15, v65, v73
	v_fmac_f32_e32 v15, v66, v74
	v_fmac_f32_e32 v15, v67, v75
	v_fmac_f32_e32 v15, v68, v76
	v_fmac_f32_e32 v15, v69, v77
	v_fmac_f32_e32 v15, v70, v78
	v_fmac_f32_e32 v15, v71, v79
	v_fmac_f32_e32 v15, v80, v88
	v_fmac_f32_e32 v15, v81, v89
	v_fmac_f32_e32 v15, v82, v90
	v_fmac_f32_e32 v15, v83, v91
	v_fmac_f32_e32 v15, v84, v92
	v_fmac_f32_e32 v15, v85, v93
	v_fmac_f32_e32 v15, v86, v94
	v_fmac_f32_e32 v15, v87, v95
	v_fmac_f32_e32 v15, v96, v104
	v_fmac_f32_e32 v15, v97, v105
	v_fmac_f32_e32 v15, v98, v106
	v_fmac_f32_e32 v15, v99, v107
	v_fmac_f32_e32 v15, v100, v108
	v_fmac_f32_e32 v15, v101, v109
	v_fmac_f32_e32 v15, v102, v110
	v_fmac_f32_e32 v15, v103, v111
	v_fmac_f32_e32 v15, v112, v120
	v_fmac_f32_e32 v15, v113, v121
	v_fmac_f32_e32 v15, v114, v122
	v_fmac_f32_e32 v15, v115, v123
	v_fmac_f32_e32 v15, v116, v124
	v_fmac_f32_e32 v15, v117, v125
	v_fmac_f32_e32 v15, v118, v126
	v_fmac_f32_e32 v15, v119, v127
	s_cmpk_eq_i32 s12, 0x200
	s_cbranch_scc0 .LBB0_81
	s_nop 0
	s_nop 0
	s_nop 0
	s_nop 0
	s_nop 0
	s_nop 0
	s_nop 0
	s_nop 0
	s_nop 0
	s_nop 0
	s_nop 0
	s_nop 0
	s_nop 0
	s_nop 0
	s_nop 0
	s_nop 0
	s_nop 0
	s_nop 0
	s_nop 0
	s_nop 0
	s_nop 0
	s_nop 0
	s_nop 0
	s_nop 0
	s_nop 0
	s_nop 0
	s_nop 0
	s_nop 0
	ds_bpermute_b32 v6, v11, v15
	s_waitcnt lgkmcnt(0)
	v_add_f32_e32 v6, v15, v6
	ds_bpermute_b32 v7, v12, v6
	s_waitcnt lgkmcnt(0)
	v_add_f32_e32 v6, v6, v7
	ds_bpermute_b32 v7, v13, v6
	s_waitcnt lgkmcnt(0)
	v_add_f32_e32 v6, v6, v7
	ds_bpermute_b32 v7, v14, v6
	s_and_saveexec_b64 s[12:13], s[0:1]
	s_cbranch_execz .LBB0_79
	v_lshl_or_b32 v8, s14, 2, v1
	v_ashrrev_i32_e32 v9, 31, v8
	v_readlane_b32 s36, v253, 16
	v_lshlrev_b64 v[8:9], 2, v[8:9]
	v_readlane_b32 s38, v253, 18
	v_readlane_b32 s39, v253, 19
	s_waitcnt lgkmcnt(0)
	v_add_f32_e32 v6, v6, v7
	v_readlane_b32 s37, v253, 17
	v_lshl_add_u64 v[16:17], s[38:39], 0, v[8:9]
	global_load_dword v15, v[16:17], off
	v_lshl_add_u64 v[8:9], s[8:9], 0, v[8:9]
	v_readlane_b32 s40, v253, 20
	v_readlane_b32 s41, v253, 21
	v_readlane_b32 s42, v253, 22
	v_readlane_b32 s43, v253, 23
	v_readlane_b32 s44, v253, 24
	v_readlane_b32 s45, v253, 25
	v_readlane_b32 s46, v253, 26
	v_readlane_b32 s47, v253, 27
	v_readlane_b32 s48, v253, 28
	v_readlane_b32 s49, v253, 29
	v_readlane_b32 s50, v253, 30
	v_readlane_b32 s51, v253, 31
	s_waitcnt vmcnt(0)
	v_add_f32_e32 v6, v6, v15
	flat_store_dword v[8:9], v6 sc1
	s_branch .LBB0_79
